# conv tile: stage/tap-loop waits no longer drain tap-weight and next-pool-tile loads; MoE position flush issues its eight atomics together; SwiGLU up-GEMM row scales prefetched in the K-loop so the epi
# baseline (speedup 1.0000x reference)
.LBB0_1174:
	s_lshl_b32 s100, s26, 8
	s_add_i32 s100, s100, s6
	v_and_or_b32 v248, v234, 15, s100
	v_ashrrev_i32_e32 v249, 31, v248
	v_lshl_add_u64 v[248:249], v[248:249], 2, s[12:13]
	global_load_dword v240, v[248:249], off
	global_load_dword v241, v[248:249], off offset:64
	global_load_dword v242, v[248:249], off offset:128
	global_load_dword v243, v[248:249], off offset:192
	global_load_dword v244, v[248:249], off offset:512
	global_load_dword v245, v[248:249], off offset:576
	global_load_dword v246, v[248:249], off offset:640
	global_load_dword v247, v[248:249], off offset:704
	ds_read_b128 v[146:149], v140
	ds_read_b128 v[150:153], v140 offset:1024
	ds_read_b128 v[154:157], v140 offset:2048
	ds_read_b128 v[158:161], v140 offset:3072
	ds_read_b128 v[162:165], v141
	ds_read_b128 v[166:169], v141 offset:1024
	ds_read_b128 v[170:173], v141 offset:2048
	ds_read_b128 v[174:177], v141 offset:3072
	s_add_u32 s30, s34, 0xfffe0080
	s_addc_u32 s31, s35, -1
	s_cmp_eq_u32 s5, 4
	s_cselect_b32 s37, s17, s31
	s_cselect_b32 s36, vcc_lo, s30
	s_cselect_b32 s31, s21, s54
	s_cselect_b32 s30, vcc_hi, s74
	s_mov_b32 m0, s27
	v_lshl_add_u64 v[210:211], s[34:35], 0, v[136:137]
	ds_read_b128 v[178:181], v145
	ds_read_b128 v[182:185], v145 offset:1024
	ds_read_b128 v[186:189], v145 offset:2048
	ds_read_b128 v[190:193], v145 offset:3072
	ds_read_b128 v[194:197], v145 offset:4096
	ds_read_b128 v[198:201], v145 offset:5120
	ds_read_b128 v[202:205], v145 offset:6144
	ds_read_b128 v[206:209], v145 offset:7168
	global_load_lds_dwordx4 v[210:211], off
	v_lshl_add_u64 v[210:211], s[34:35], 0, v[138:139]
	s_mov_b32 m0, s90
	s_nop 0
	global_load_lds_dwordx4 v[210:211], off
	s_waitcnt vmcnt(16)
	s_waitcnt lgkmcnt(0)
	s_barrier
	s_setprio 1
	s_waitcnt lgkmcnt(0)
	v_mfma_i32_16x16x64_i8 v[122:125], v[146:149], v[178:181], v[122:125]
	v_mfma_i32_16x16x64_i8 v[118:121], v[154:157], v[178:181], v[118:121]
	v_mfma_i32_16x16x64_i8 v[106:109], v[146:149], v[186:189], v[106:109]
	v_mfma_i32_16x16x64_i8 v[102:105], v[154:157], v[186:189], v[102:105]
	v_mfma_i32_16x16x64_i8 v[90:93], v[146:149], v[194:197], v[90:93]
	v_mfma_i32_16x16x64_i8 v[86:89], v[154:157], v[194:197], v[86:89]
	v_mfma_i32_16x16x64_i8 v[74:77], v[146:149], v[202:205], v[74:77]
	v_mfma_i32_16x16x64_i8 v[70:73], v[154:157], v[202:205], v[70:73]
	v_mfma_i32_16x16x64_i8 v[122:125], v[150:153], v[182:185], v[122:125]
	v_mfma_i32_16x16x64_i8 v[118:121], v[158:161], v[182:185], v[118:121]
	v_mfma_i32_16x16x64_i8 v[106:109], v[150:153], v[190:193], v[106:109]
	v_mfma_i32_16x16x64_i8 v[102:105], v[158:161], v[190:193], v[102:105]
	v_mfma_i32_16x16x64_i8 v[90:93], v[150:153], v[198:201], v[90:93]
	v_mfma_i32_16x16x64_i8 v[86:89], v[158:161], v[198:201], v[86:89]
	v_mfma_i32_16x16x64_i8 v[74:77], v[150:153], v[206:209], v[74:77]
	v_mfma_i32_16x16x64_i8 v[70:73], v[158:161], v[206:209], v[70:73]
	s_setprio 0
	s_setprio 1
	v_mfma_i32_16x16x64_i8 v[126:129], v[162:165], v[178:181], v[126:129]
	v_mfma_i32_16x16x64_i8 v[114:117], v[170:173], v[178:181], v[114:117]
	v_mfma_i32_16x16x64_i8 v[110:113], v[162:165], v[186:189], v[110:113]
	v_mfma_i32_16x16x64_i8 v[98:101], v[170:173], v[186:189], v[98:101]
	v_mfma_i32_16x16x64_i8 v[94:97], v[162:165], v[194:197], v[94:97]
	v_mfma_i32_16x16x64_i8 v[82:85], v[170:173], v[194:197], v[82:85]
	v_mfma_i32_16x16x64_i8 v[78:81], v[162:165], v[202:205], v[78:81]
	v_mfma_i32_16x16x64_i8 v[66:69], v[170:173], v[202:205], v[66:69]
	v_mfma_i32_16x16x64_i8 v[126:129], v[166:169], v[182:185], v[126:129]
	v_mfma_i32_16x16x64_i8 v[114:117], v[174:177], v[182:185], v[114:117]
	v_mfma_i32_16x16x64_i8 v[110:113], v[166:169], v[190:193], v[110:113]
	v_mfma_i32_16x16x64_i8 v[98:101], v[174:177], v[190:193], v[98:101]
	v_mfma_i32_16x16x64_i8 v[94:97], v[166:169], v[198:201], v[94:97]
	v_mfma_i32_16x16x64_i8 v[82:85], v[174:177], v[198:201], v[82:85]
	v_mfma_i32_16x16x64_i8 v[78:81], v[166:169], v[206:209], v[78:81]
	v_mfma_i32_16x16x64_i8 v[66:69], v[174:177], v[206:209], v[66:69]
	s_setprio 0
	s_barrier
	s_mov_b32 m0, s50
	v_lshl_add_u64 v[210:211], s[30:31], 0, v[0:1]
	s_add_u32 s76, s30, 0x20000
	ds_read_b128 v[178:181], v145 offset:16384
	ds_read_b128 v[182:185], v145 offset:17408
	ds_read_b128 v[186:189], v145 offset:18432
	ds_read_b128 v[190:193], v145 offset:19456
	ds_read_b128 v[194:197], v145 offset:20480
	ds_read_b128 v[198:201], v145 offset:21504
	ds_read_b128 v[202:205], v145 offset:22528
	ds_read_b128 v[206:209], v145 offset:23552
	global_load_lds_dwordx4 v[210:211], off
	v_lshl_add_u64 v[212:213], s[30:31], 0, v[134:135]
	s_mov_b32 m0, s51
	s_addc_u32 s77, s31, 0
	global_load_lds_dwordx4 v[212:213], off
	v_lshl_add_u64 v[214:215], s[76:77], 0, v[0:1]
	s_mov_b32 m0, s94
	v_lshl_add_u64 v[216:217], s[36:37], 0, v[132:133]
	global_load_lds_dwordx4 v[214:215], off
	v_lshl_add_u64 v[214:215], s[76:77], 0, v[134:135]
	s_mov_b32 m0, s95
	s_nop 0
	global_load_lds_dwordx4 v[214:215], off
	v_lshl_add_u64 v[214:215], s[36:37], 0, v[130:131]
	s_mov_b32 m0, s4
	s_nop 0
	global_load_lds_dwordx4 v[214:215], off
	s_mov_b32 m0, s29
	s_nop 0
	global_load_lds_dwordx4 v[216:217], off
	s_waitcnt vmcnt(16)
	s_waitcnt lgkmcnt(0)
	s_barrier
	s_setprio 1
	s_waitcnt lgkmcnt(0)
	v_mfma_i32_16x16x64_i8 v[58:61], v[146:149], v[178:181], v[58:61]
	v_mfma_i32_16x16x64_i8 v[54:57], v[154:157], v[178:181], v[54:57]
	v_mfma_i32_16x16x64_i8 v[42:45], v[146:149], v[186:189], v[42:45]
	v_mfma_i32_16x16x64_i8 v[38:41], v[154:157], v[186:189], v[38:41]
	v_mfma_i32_16x16x64_i8 v[26:29], v[146:149], v[194:197], v[26:29]
	v_mfma_i32_16x16x64_i8 v[22:25], v[154:157], v[194:197], v[22:25]
	v_mfma_i32_16x16x64_i8 v[10:13], v[146:149], v[202:205], v[10:13]
	v_mfma_i32_16x16x64_i8 v[6:9], v[154:157], v[202:205], v[6:9]
	v_mfma_i32_16x16x64_i8 v[58:61], v[150:153], v[182:185], v[58:61]
	v_mfma_i32_16x16x64_i8 v[54:57], v[158:161], v[182:185], v[54:57]
	v_mfma_i32_16x16x64_i8 v[42:45], v[150:153], v[190:193], v[42:45]
	v_mfma_i32_16x16x64_i8 v[38:41], v[158:161], v[190:193], v[38:41]
	v_mfma_i32_16x16x64_i8 v[26:29], v[150:153], v[198:201], v[26:29]
	v_mfma_i32_16x16x64_i8 v[22:25], v[158:161], v[198:201], v[22:25]
	v_mfma_i32_16x16x64_i8 v[10:13], v[150:153], v[206:209], v[10:13]
	v_mfma_i32_16x16x64_i8 v[6:9], v[158:161], v[206:209], v[6:9]
	s_setprio 0
	s_setprio 1
	v_mfma_i32_16x16x64_i8 v[62:65], v[162:165], v[178:181], v[62:65]
	v_mfma_i32_16x16x64_i8 v[50:53], v[170:173], v[178:181], v[50:53]
	v_mfma_i32_16x16x64_i8 v[46:49], v[162:165], v[186:189], v[46:49]
	v_mfma_i32_16x16x64_i8 v[34:37], v[170:173], v[186:189], v[34:37]
	v_mfma_i32_16x16x64_i8 v[30:33], v[162:165], v[194:197], v[30:33]
	v_mfma_i32_16x16x64_i8 v[18:21], v[170:173], v[194:197], v[18:21]
	v_mfma_i32_16x16x64_i8 v[14:17], v[162:165], v[202:205], v[14:17]
	v_mfma_i32_16x16x64_i8 v[2:5], v[170:173], v[202:205], v[2:5]
	v_mfma_i32_16x16x64_i8 v[62:65], v[166:169], v[182:185], v[62:65]
	v_mfma_i32_16x16x64_i8 v[50:53], v[174:177], v[182:185], v[50:53]
	v_mfma_i32_16x16x64_i8 v[46:49], v[166:169], v[190:193], v[46:49]
	v_mfma_i32_16x16x64_i8 v[34:37], v[174:177], v[190:193], v[34:37]
	v_mfma_i32_16x16x64_i8 v[30:33], v[166:169], v[198:201], v[30:33]
	v_mfma_i32_16x16x64_i8 v[18:21], v[174:177], v[198:201], v[18:21]
	v_mfma_i32_16x16x64_i8 v[14:17], v[166:169], v[206:209], v[14:17]
	v_mfma_i32_16x16x64_i8 v[2:5], v[174:177], v[206:209], v[2:5]
	s_setprio 0
	s_barrier
	ds_read_b128 v[146:149], v142
	ds_read_b128 v[150:153], v142 offset:1024
	ds_read_b128 v[154:157], v142 offset:2048
	ds_read_b128 v[158:161], v142 offset:3072
	ds_read_b128 v[162:165], v143
	ds_read_b128 v[166:169], v143 offset:1024
	ds_read_b128 v[170:173], v143 offset:2048
	ds_read_b128 v[174:177], v143 offset:3072
	s_add_u32 s36, s36, 0x20000
	s_addc_u32 s37, s37, 0
	s_mov_b32 m0, s96
	v_lshl_add_u64 v[218:219], s[36:37], 0, v[130:131]
	ds_read_b128 v[178:181], v145 offset:32768
	ds_read_b128 v[182:185], v145 offset:33792
	ds_read_b128 v[186:189], v145 offset:34816
	ds_read_b128 v[190:193], v145 offset:35840
	ds_read_b128 v[194:197], v145 offset:36864
	ds_read_b128 v[198:201], v145 offset:37888
	ds_read_b128 v[202:205], v145 offset:38912
	ds_read_b128 v[206:209], v145 offset:39936
	global_load_lds_dwordx4 v[218:219], off
	v_lshl_add_u64 v[218:219], s[36:37], 0, v[132:133]
	s_mov_b32 m0, s44
	s_nop 0
	global_load_lds_dwordx4 v[218:219], off
	s_waitcnt vmcnt(8)
	s_waitcnt lgkmcnt(0)
	s_barrier
	s_setprio 1
	s_waitcnt lgkmcnt(0)
	v_mfma_i32_16x16x64_i8 v[122:125], v[146:149], v[178:181], v[122:125]
	v_mfma_i32_16x16x64_i8 v[118:121], v[154:157], v[178:181], v[118:121]
	v_mfma_i32_16x16x64_i8 v[106:109], v[146:149], v[186:189], v[106:109]
	v_mfma_i32_16x16x64_i8 v[102:105], v[154:157], v[186:189], v[102:105]
	v_mfma_i32_16x16x64_i8 v[90:93], v[146:149], v[194:197], v[90:93]
	v_mfma_i32_16x16x64_i8 v[86:89], v[154:157], v[194:197], v[86:89]
	v_mfma_i32_16x16x64_i8 v[74:77], v[146:149], v[202:205], v[74:77]
	v_mfma_i32_16x16x64_i8 v[70:73], v[154:157], v[202:205], v[70:73]
	v_mfma_i32_16x16x64_i8 v[122:125], v[150:153], v[182:185], v[122:125]
	v_mfma_i32_16x16x64_i8 v[118:121], v[158:161], v[182:185], v[118:121]
	v_mfma_i32_16x16x64_i8 v[106:109], v[150:153], v[190:193], v[106:109]
	v_mfma_i32_16x16x64_i8 v[102:105], v[158:161], v[190:193], v[102:105]
	v_mfma_i32_16x16x64_i8 v[90:93], v[150:153], v[198:201], v[90:93]
	v_mfma_i32_16x16x64_i8 v[86:89], v[158:161], v[198:201], v[86:89]
	v_mfma_i32_16x16x64_i8 v[74:77], v[150:153], v[206:209], v[74:77]
	v_mfma_i32_16x16x64_i8 v[70:73], v[158:161], v[206:209], v[70:73]
	s_setprio 0
	s_setprio 1
	v_mfma_i32_16x16x64_i8 v[126:129], v[162:165], v[178:181], v[126:129]
	v_mfma_i32_16x16x64_i8 v[114:117], v[170:173], v[178:181], v[114:117]
	v_mfma_i32_16x16x64_i8 v[110:113], v[162:165], v[186:189], v[110:113]
	v_mfma_i32_16x16x64_i8 v[98:101], v[170:173], v[186:189], v[98:101]
	v_mfma_i32_16x16x64_i8 v[94:97], v[162:165], v[194:197], v[94:97]
	v_mfma_i32_16x16x64_i8 v[82:85], v[170:173], v[194:197], v[82:85]
	v_mfma_i32_16x16x64_i8 v[78:81], v[162:165], v[202:205], v[78:81]
	v_mfma_i32_16x16x64_i8 v[66:69], v[170:173], v[202:205], v[66:69]
	v_mfma_i32_16x16x64_i8 v[126:129], v[166:169], v[182:185], v[126:129]
	v_mfma_i32_16x16x64_i8 v[114:117], v[174:177], v[182:185], v[114:117]
	v_mfma_i32_16x16x64_i8 v[110:113], v[166:169], v[190:193], v[110:113]
	v_mfma_i32_16x16x64_i8 v[98:101], v[174:177], v[190:193], v[98:101]
	v_mfma_i32_16x16x64_i8 v[94:97], v[166:169], v[198:201], v[94:97]
	v_mfma_i32_16x16x64_i8 v[82:85], v[174:177], v[198:201], v[82:85]
	v_mfma_i32_16x16x64_i8 v[78:81], v[166:169], v[206:209], v[78:81]
	v_mfma_i32_16x16x64_i8 v[66:69], v[174:177], v[206:209], v[66:69]
	s_setprio 0
	s_barrier
	s_mov_b32 m0, s78
	v_lshl_add_u64 v[210:211], v[210:211], 0, s[56:57]
	s_add_u32 s30, s30, 0x20080
	ds_read_b128 v[178:181], v145 offset:49152
	ds_read_b128 v[182:185], v145 offset:50176
	ds_read_b128 v[186:189], v145 offset:51200
	ds_read_b128 v[190:193], v145 offset:52224
	ds_read_b128 v[194:197], v145 offset:53248
	ds_read_b128 v[198:201], v145 offset:54272
	ds_read_b128 v[202:205], v145 offset:55296
	ds_read_b128 v[206:209], v145 offset:56320
	global_load_lds_dwordx4 v[210:211], off
	v_lshl_add_u64 v[210:211], v[212:213], 0, s[56:57]
	s_mov_b32 m0, s79
	s_addc_u32 s31, s31, 0
	global_load_lds_dwordx4 v[210:211], off
	v_lshl_add_u64 v[210:211], s[30:31], 0, v[0:1]
	s_mov_b32 m0, s58
	s_nop 0
	global_load_lds_dwordx4 v[210:211], off
	v_lshl_add_u64 v[210:211], s[30:31], 0, v[134:135]
	s_mov_b32 m0, s48
	s_nop 0
	global_load_lds_dwordx4 v[210:211], off
	v_lshl_add_u64 v[210:211], v[214:215], 0, s[56:57]
	s_mov_b32 m0, s88
	s_nop 0
	global_load_lds_dwordx4 v[210:211], off
	v_lshl_add_u64 v[210:211], v[216:217], 0, s[56:57]
	s_mov_b32 m0, s89
	s_nop 0
	global_load_lds_dwordx4 v[210:211], off
	s_waitcnt vmcnt(8)
	s_waitcnt lgkmcnt(0)
	s_barrier
	s_setprio 1
	s_waitcnt lgkmcnt(0)
	v_mfma_i32_16x16x64_i8 v[58:61], v[146:149], v[178:181], v[58:61]
	v_mfma_i32_16x16x64_i8 v[54:57], v[154:157], v[178:181], v[54:57]
	v_mfma_i32_16x16x64_i8 v[42:45], v[146:149], v[186:189], v[42:45]
	v_mfma_i32_16x16x64_i8 v[38:41], v[154:157], v[186:189], v[38:41]
	v_mfma_i32_16x16x64_i8 v[26:29], v[146:149], v[194:197], v[26:29]
	v_mfma_i32_16x16x64_i8 v[22:25], v[154:157], v[194:197], v[22:25]
	v_mfma_i32_16x16x64_i8 v[10:13], v[146:149], v[202:205], v[10:13]
	v_mfma_i32_16x16x64_i8 v[6:9], v[154:157], v[202:205], v[6:9]
	v_mfma_i32_16x16x64_i8 v[58:61], v[150:153], v[182:185], v[58:61]
	v_mfma_i32_16x16x64_i8 v[54:57], v[158:161], v[182:185], v[54:57]
	v_mfma_i32_16x16x64_i8 v[42:45], v[150:153], v[190:193], v[42:45]
	v_mfma_i32_16x16x64_i8 v[38:41], v[158:161], v[190:193], v[38:41]
	v_mfma_i32_16x16x64_i8 v[26:29], v[150:153], v[198:201], v[26:29]
	v_mfma_i32_16x16x64_i8 v[22:25], v[158:161], v[198:201], v[22:25]
	v_mfma_i32_16x16x64_i8 v[10:13], v[150:153], v[206:209], v[10:13]
	v_mfma_i32_16x16x64_i8 v[6:9], v[158:161], v[206:209], v[6:9]
	s_setprio 0
	s_setprio 1
	v_mfma_i32_16x16x64_i8 v[62:65], v[162:165], v[178:181], v[62:65]
	v_mfma_i32_16x16x64_i8 v[50:53], v[170:173], v[178:181], v[50:53]
	v_mfma_i32_16x16x64_i8 v[46:49], v[162:165], v[186:189], v[46:49]
	v_mfma_i32_16x16x64_i8 v[34:37], v[170:173], v[186:189], v[34:37]
	v_mfma_i32_16x16x64_i8 v[30:33], v[162:165], v[194:197], v[30:33]
	v_mfma_i32_16x16x64_i8 v[18:21], v[170:173], v[194:197], v[18:21]
	v_mfma_i32_16x16x64_i8 v[14:17], v[162:165], v[202:205], v[14:17]
	v_mfma_i32_16x16x64_i8 v[2:5], v[170:173], v[202:205], v[2:5]
	v_mfma_i32_16x16x64_i8 v[62:65], v[166:169], v[182:185], v[62:65]
	v_mfma_i32_16x16x64_i8 v[50:53], v[174:177], v[182:185], v[50:53]
	v_mfma_i32_16x16x64_i8 v[46:49], v[166:169], v[190:193], v[46:49]
	v_mfma_i32_16x16x64_i8 v[34:37], v[174:177], v[190:193], v[34:37]
	v_mfma_i32_16x16x64_i8 v[30:33], v[166:169], v[198:201], v[30:33]
	v_mfma_i32_16x16x64_i8 v[18:21], v[174:177], v[198:201], v[18:21]
	v_mfma_i32_16x16x64_i8 v[14:17], v[166:169], v[206:209], v[14:17]
	v_mfma_i32_16x16x64_i8 v[2:5], v[174:177], v[206:209], v[2:5]
	s_setprio 0
	s_barrier
	s_add_i32 s5, s5, 2
	s_add_u32 s34, s34, 0x100
	s_addc_u32 s35, s35, 0
	s_add_u32 s74, s74, 0x100
	s_addc_u32 s54, s54, 0
	s_cmp_gt_u32 s5, 5
	s_cbranch_scc0 .LBB0_1174
	s_lshl_b32 s5, s26, 8
	s_add_i32 s5, s5, s6
	v_mbcnt_lo_u32_b32 v140, -1, 0
	v_mbcnt_hi_u32_b32 v140, -1, v140
	v_readlane_b32 s78, v255, 13
	v_and_or_b32 v142, v140, 15, s5
	v_ashrrev_i32_e32 v143, 31, v142
	v_lshl_add_u64 v[152:153], v[142:143], 2, s[12:13]
	v_mov_b32_e32 v141, v240
	v_mov_b32_e32 v143, v241
	v_mov_b32_e32 v146, v242
	v_mov_b32_e32 v147, v243
	v_mov_b32_e32 v149, v244
	v_mov_b32_e32 v150, v245
	v_mov_b32_e32 v151, v246
	v_mov_b32_e32 v152, v247
	s_and_b64 vcc, exec, s[14:15]
	v_readlane_b32 s79, v255, 14
	s_movk_i32 s74, 0x1000
	s_mov_b64 s[94:95], 0x1000
	s_cbranch_vccz .LBB0_1177
	s_barrier
.LBB0_1177:
	v_cvt_f32_i32_e32 v123, v123
	v_cvt_f32_i32_e32 v122, v122
	v_cvt_f32_i32_e32 v125, v125
	v_cvt_f32_i32_e32 v124, v124
	v_cvt_f32_i32_e32 v119, v119
	v_cvt_f32_i32_e32 v118, v118
	v_cvt_f32_i32_e32 v121, v121
	v_cvt_f32_i32_e32 v120, v120
	s_waitcnt vmcnt(8)
	v_mul_f32_e32 v158, 0x3a800000, v141
	v_mul_f32_e32 v161, 0x3a800000, v147
	v_mul_f32_e32 v147, 0x3a800000, v150
	v_mul_f32_e32 v150, 0xbfb8aa3b, v158
	v_pk_mul_f32 v[154:155], v[150:151], v[122:123] op_sel_hi:[0,1]
	v_mul_f32_e32 v159, 0x3a800000, v143
	v_mul_f32_e32 v160, 0x3a800000, v146
	v_mul_f32_e32 v146, 0x3a800000, v151
	v_mul_f32_e32 v143, 0x3a800000, v152
	v_pk_mul_f32 v[152:153], v[150:151], v[124:125] op_sel_hi:[0,1]
	v_pk_mul_f32 v[156:157], v[150:151], v[120:121] op_sel_hi:[0,1]
	v_pk_mul_f32 v[150:151], v[150:151], v[118:119] op_sel_hi:[0,1]
	v_exp_f32_e32 v154, v154
	v_exp_f32_e32 v155, v155
	v_exp_f32_e32 v150, v150
	v_exp_f32_e32 v151, v151
	v_exp_f32_e32 v156, v156
	v_exp_f32_e32 v157, v157
	v_pk_add_f32 v[154:155], v[154:155], 1.0 op_sel_hi:[1,0]
	v_cvt_f32_i32_e32 v127, v127
	v_cvt_f32_i32_e32 v126, v126
	v_exp_f32_e32 v152, v152
	v_exp_f32_e32 v153, v153
	v_pk_add_f32 v[156:157], v[156:157], 1.0 op_sel_hi:[1,0]
	v_pk_add_f32 v[150:151], v[150:151], 1.0 op_sel_hi:[1,0]
	v_rcp_f32_e32 v154, v154
	v_rcp_f32_e32 v155, v155
	v_cvt_f32_i32_e32 v117, v117
	v_cvt_f32_i32_e32 v116, v116
	v_cvt_f32_i32_e32 v115, v115
	v_cvt_f32_i32_e32 v114, v114
	v_rcp_f32_e32 v150, v150
	v_rcp_f32_e32 v151, v151
	v_rcp_f32_e32 v156, v156
	v_rcp_f32_e32 v157, v157
	v_mul_f32_e32 v158, v158, v158
	v_pk_add_f32 v[152:153], v[152:153], 1.0 op_sel_hi:[1,0]
	v_pk_mul_f32 v[122:123], v[122:123], v[126:127]
	v_pk_mul_f32 v[126:127], v[158:159], v[154:155] op_sel_hi:[0,1]
	s_mul_hi_i32 s5, s28, 0x92492493
	v_cvt_f32_i32_e32 v129, v129
	v_cvt_f32_i32_e32 v128, v128
	v_rcp_f32_e32 v152, v152
	v_rcp_f32_e32 v153, v153
	v_pk_mul_f32 v[122:123], v[122:123], v[126:127]
	v_pk_mul_f32 v[114:115], v[118:119], v[114:115]
	v_pk_mul_f32 v[116:117], v[120:121], v[116:117]
	v_pk_mul_f32 v[118:119], v[158:159], v[150:151] op_sel_hi:[0,1]
	v_pk_mul_f32 v[120:121], v[158:159], v[156:157] op_sel_hi:[0,1]
	s_add_i32 s5, s5, s28
	v_pk_mul_f32 v[116:117], v[116:117], v[120:121]
	v_pk_mul_f32 v[114:115], v[114:115], v[118:119]
	v_med3_f32 v119, v122, s61, v237
	v_med3_f32 v120, v123, s61, v237
	v_mov_b32_e32 v118, v1
	s_lshr_b32 s17, s5, 31
	s_lshr_b32 s5, s5, 4
	v_cvt_pk_fp8_f32 v118, v119, v120
	v_med3_f32 v114, v114, s61, v237
	v_med3_f32 v115, v115, s61, v237
	v_mov_b32_e32 v119, v1
	s_add_i32 s5, s5, s17
	v_cvt_pk_fp8_f32 v119, v114, v115
	s_mul_i32 s5, s5, 28
	v_pk_mul_f32 v[124:125], v[124:125], v[128:129]
	v_pk_mul_f32 v[128:129], v[158:159], v[152:153] op_sel_hi:[0,1]
	s_sub_i32 s5, s28, s5
	v_pk_mul_f32 v[124:125], v[124:125], v[128:129]
	v_ashrrev_i32_e32 v140, 1, v140
	s_lshl_b32 s5, s5, 7
	v_med3_f32 v121, v124, s61, v237
	v_med3_f32 v122, v125, s61, v237
	v_med3_f32 v114, v116, s61, v237
	v_med3_f32 v115, v117, s61, v237
	v_and_b32_e32 v140, -8, v140
	s_or_b32 s5, s5, s7
	v_cvt_pk_fp8_f32 v118, v121, v122 op_sel:[0,0,1]
	v_cvt_pk_fp8_f32 v119, v114, v115 op_sel:[0,0,1]
	v_add_u32_e32 v140, s5, v140
	v_mov_b64_e32 v[114:115], s[10:11]
	s_movk_i32 s5, 0xe00
	v_cvt_f32_i32_e32 v107, v107
	v_cvt_f32_i32_e32 v106, v106
	v_ashrrev_i32_e32 v141, 31, v140
	v_mad_i64_i32 v[116:117], s[26:27], v142, s5, v[114:115]
	v_cvt_f32_i32_e32 v109, v109
	v_cvt_f32_i32_e32 v108, v108
	v_cvt_f32_i32_e32 v103, v103
	v_cvt_f32_i32_e32 v102, v102
	v_cvt_f32_i32_e32 v105, v105
	v_cvt_f32_i32_e32 v104, v104
	v_lshl_add_u64 v[116:117], v[116:117], 0, v[140:141]
	global_store_dwordx2 v[116:117], v[118:119], off
	v_mul_f32_e32 v116, 0xbfb8aa3b, v159
	v_pk_mul_f32 v[120:121], v[116:117], v[106:107] op_sel_hi:[0,1]
	v_pk_mul_f32 v[118:119], v[116:117], v[108:109] op_sel_hi:[0,1]
	v_pk_mul_f32 v[122:123], v[116:117], v[104:105] op_sel_hi:[0,1]
	v_pk_mul_f32 v[116:117], v[116:117], v[102:103] op_sel_hi:[0,1]
	v_exp_f32_e32 v120, v120
	v_exp_f32_e32 v121, v121
	v_exp_f32_e32 v116, v116
	v_exp_f32_e32 v117, v117
	v_exp_f32_e32 v122, v122
	v_exp_f32_e32 v123, v123
	v_pk_add_f32 v[120:121], v[120:121], 1.0 op_sel_hi:[1,0]
	v_cvt_f32_i32_e32 v111, v111
	v_cvt_f32_i32_e32 v110, v110
	v_exp_f32_e32 v118, v118
	v_exp_f32_e32 v119, v119
	v_pk_add_f32 v[122:123], v[122:123], 1.0 op_sel_hi:[1,0]
	v_pk_add_f32 v[116:117], v[116:117], 1.0 op_sel_hi:[1,0]
	v_rcp_f32_e32 v120, v120
	v_rcp_f32_e32 v121, v121
	v_cvt_f32_i32_e32 v101, v101
	v_cvt_f32_i32_e32 v100, v100
	v_cvt_f32_i32_e32 v99, v99
	v_cvt_f32_i32_e32 v98, v98
	v_rcp_f32_e32 v116, v116
	v_rcp_f32_e32 v117, v117
	v_rcp_f32_e32 v122, v122
	v_rcp_f32_e32 v123, v123
	v_or_b32_e32 v125, 16, v142
	v_mul_f32_e32 v124, v159, v159
	v_pk_add_f32 v[118:119], v[118:119], 1.0 op_sel_hi:[1,0]
	v_pk_mul_f32 v[106:107], v[106:107], v[110:111]
	v_pk_mul_f32 v[110:111], v[124:125], v[120:121] op_sel_hi:[0,1]
	v_cvt_f32_i32_e32 v113, v113
	v_cvt_f32_i32_e32 v112, v112
	v_rcp_f32_e32 v118, v118
	v_rcp_f32_e32 v119, v119
	v_pk_mul_f32 v[106:107], v[106:107], v[110:111]
	v_pk_mul_f32 v[98:99], v[102:103], v[98:99]
	v_pk_mul_f32 v[100:101], v[104:105], v[100:101]
	v_pk_mul_f32 v[102:103], v[124:125], v[116:117] op_sel_hi:[0,1]
	v_pk_mul_f32 v[104:105], v[124:125], v[122:123] op_sel_hi:[0,1]
	v_pk_mul_f32 v[100:101], v[100:101], v[104:105]
	v_pk_mul_f32 v[98:99], v[98:99], v[102:103]
	v_med3_f32 v103, v106, s61, v237
	v_med3_f32 v104, v107, s61, v237
	v_mov_b32_e32 v102, v1
	v_cvt_pk_fp8_f32 v102, v103, v104
	v_med3_f32 v98, v98, s61, v237
	v_med3_f32 v99, v99, s61, v237
	v_mov_b32_e32 v103, v1
	v_cvt_pk_fp8_f32 v103, v98, v99
	v_pk_mul_f32 v[108:109], v[108:109], v[112:113]
	v_pk_mul_f32 v[112:113], v[124:125], v[118:119] op_sel_hi:[0,1]
	v_pk_mul_f32 v[108:109], v[108:109], v[112:113]
	v_med3_f32 v98, v100, s61, v237
	v_med3_f32 v105, v108, s61, v237
	v_med3_f32 v106, v109, s61, v237
	v_med3_f32 v99, v101, s61, v237
	v_cvt_pk_fp8_f32 v102, v105, v106 op_sel:[0,0,1]
	v_cvt_pk_fp8_f32 v103, v98, v99 op_sel:[0,0,1]
	v_cvt_f32_i32_e32 v91, v91
	v_cvt_f32_i32_e32 v90, v90
	v_mad_i64_i32 v[98:99], s[26:27], v125, s5, v[114:115]
	v_cvt_f32_i32_e32 v93, v93
	v_cvt_f32_i32_e32 v92, v92
	v_cvt_f32_i32_e32 v87, v87
	v_cvt_f32_i32_e32 v86, v86
	v_cvt_f32_i32_e32 v89, v89
	v_cvt_f32_i32_e32 v88, v88
	v_lshl_add_u64 v[98:99], v[98:99], 0, v[140:141]
	global_store_dwordx2 v[98:99], v[102:103], off
	v_mul_f32_e32 v98, 0xbfb8aa3b, v160
	v_pk_mul_f32 v[102:103], v[98:99], v[90:91] op_sel_hi:[0,1]
	v_pk_mul_f32 v[100:101], v[98:99], v[92:93] op_sel_hi:[0,1]
	v_pk_mul_f32 v[104:105], v[98:99], v[88:89] op_sel_hi:[0,1]
	v_pk_mul_f32 v[98:99], v[98:99], v[86:87] op_sel_hi:[0,1]
	v_exp_f32_e32 v102, v102
	v_exp_f32_e32 v103, v103
	v_exp_f32_e32 v98, v98
	v_exp_f32_e32 v99, v99
	v_exp_f32_e32 v104, v104
	v_exp_f32_e32 v105, v105
	v_pk_add_f32 v[102:103], v[102:103], 1.0 op_sel_hi:[1,0]
	v_cvt_f32_i32_e32 v95, v95
	v_cvt_f32_i32_e32 v94, v94
	v_exp_f32_e32 v100, v100
	v_exp_f32_e32 v101, v101
	v_pk_add_f32 v[104:105], v[104:105], 1.0 op_sel_hi:[1,0]
	v_pk_add_f32 v[98:99], v[98:99], 1.0 op_sel_hi:[1,0]
	v_rcp_f32_e32 v102, v102
	v_rcp_f32_e32 v103, v103
	v_cvt_f32_i32_e32 v85, v85
	v_cvt_f32_i32_e32 v84, v84
	v_cvt_f32_i32_e32 v83, v83
	v_cvt_f32_i32_e32 v82, v82
	v_rcp_f32_e32 v98, v98
	v_rcp_f32_e32 v99, v99
	v_rcp_f32_e32 v104, v104
	v_rcp_f32_e32 v105, v105
	v_or_b32_e32 v107, 32, v142
	v_mul_f32_e32 v106, v160, v160
	v_pk_add_f32 v[100:101], v[100:101], 1.0 op_sel_hi:[1,0]
	v_pk_mul_f32 v[90:91], v[90:91], v[94:95]
	v_pk_mul_f32 v[94:95], v[106:107], v[102:103] op_sel_hi:[0,1]
	v_cvt_f32_i32_e32 v97, v97
	v_cvt_f32_i32_e32 v96, v96
	v_rcp_f32_e32 v100, v100
	v_rcp_f32_e32 v101, v101
	v_pk_mul_f32 v[90:91], v[90:91], v[94:95]
	v_pk_mul_f32 v[82:83], v[86:87], v[82:83]
	v_pk_mul_f32 v[84:85], v[88:89], v[84:85]
	v_pk_mul_f32 v[86:87], v[106:107], v[98:99] op_sel_hi:[0,1]
	v_pk_mul_f32 v[88:89], v[106:107], v[104:105] op_sel_hi:[0,1]
	v_pk_mul_f32 v[84:85], v[84:85], v[88:89]
	v_pk_mul_f32 v[82:83], v[82:83], v[86:87]
	v_med3_f32 v87, v90, s61, v237
	v_med3_f32 v88, v91, s61, v237
	v_mov_b32_e32 v86, v1
	v_cvt_pk_fp8_f32 v86, v87, v88
	v_med3_f32 v82, v82, s61, v237
	v_med3_f32 v83, v83, s61, v237
	v_mov_b32_e32 v87, v1
	v_cvt_pk_fp8_f32 v87, v82, v83
	v_pk_mul_f32 v[92:93], v[92:93], v[96:97]
	v_pk_mul_f32 v[96:97], v[106:107], v[100:101] op_sel_hi:[0,1]
	v_pk_mul_f32 v[92:93], v[92:93], v[96:97]
	v_med3_f32 v82, v84, s61, v237
	v_med3_f32 v89, v92, s61, v237
	v_med3_f32 v90, v93, s61, v237
	v_med3_f32 v83, v85, s61, v237
	v_cvt_pk_fp8_f32 v86, v89, v90 op_sel:[0,0,1]
	v_cvt_pk_fp8_f32 v87, v82, v83 op_sel:[0,0,1]
	v_cvt_f32_i32_e32 v75, v75
	v_cvt_f32_i32_e32 v74, v74
	v_mad_i64_i32 v[82:83], s[26:27], v107, s5, v[114:115]
	v_cvt_f32_i32_e32 v77, v77
	v_cvt_f32_i32_e32 v76, v76
	v_cvt_f32_i32_e32 v71, v71
	v_cvt_f32_i32_e32 v70, v70
	v_cvt_f32_i32_e32 v73, v73
	v_cvt_f32_i32_e32 v72, v72
	v_lshl_add_u64 v[82:83], v[82:83], 0, v[140:141]
	global_store_dwordx2 v[82:83], v[86:87], off
	v_mul_f32_e32 v82, 0xbfb8aa3b, v161
	v_pk_mul_f32 v[86:87], v[82:83], v[74:75] op_sel_hi:[0,1]
	v_pk_mul_f32 v[84:85], v[82:83], v[76:77] op_sel_hi:[0,1]
	v_pk_mul_f32 v[88:89], v[82:83], v[72:73] op_sel_hi:[0,1]
	v_pk_mul_f32 v[82:83], v[82:83], v[70:71] op_sel_hi:[0,1]
	v_exp_f32_e32 v86, v86
	v_exp_f32_e32 v87, v87
	v_exp_f32_e32 v82, v82
	v_exp_f32_e32 v83, v83
	v_exp_f32_e32 v88, v88
	v_exp_f32_e32 v89, v89
	v_pk_add_f32 v[86:87], v[86:87], 1.0 op_sel_hi:[1,0]
	v_cvt_f32_i32_e32 v79, v79
	v_cvt_f32_i32_e32 v78, v78
	v_exp_f32_e32 v84, v84
	v_exp_f32_e32 v85, v85
	v_pk_add_f32 v[88:89], v[88:89], 1.0 op_sel_hi:[1,0]
	v_pk_add_f32 v[82:83], v[82:83], 1.0 op_sel_hi:[1,0]
	v_rcp_f32_e32 v86, v86
	v_rcp_f32_e32 v87, v87
	v_cvt_f32_i32_e32 v69, v69
	v_cvt_f32_i32_e32 v68, v68
	v_cvt_f32_i32_e32 v67, v67
	v_cvt_f32_i32_e32 v66, v66
	v_rcp_f32_e32 v82, v82
	v_rcp_f32_e32 v83, v83
	v_rcp_f32_e32 v88, v88
	v_rcp_f32_e32 v89, v89
	v_or_b32_e32 v91, 48, v142
	v_mul_f32_e32 v90, v161, v161
	v_pk_add_f32 v[84:85], v[84:85], 1.0 op_sel_hi:[1,0]
	v_pk_mul_f32 v[74:75], v[74:75], v[78:79]
	v_pk_mul_f32 v[78:79], v[90:91], v[86:87] op_sel_hi:[0,1]
	v_cvt_f32_i32_e32 v81, v81
	v_cvt_f32_i32_e32 v80, v80
	v_rcp_f32_e32 v84, v84
	v_rcp_f32_e32 v85, v85
	v_pk_mul_f32 v[74:75], v[74:75], v[78:79]
	v_pk_mul_f32 v[66:67], v[70:71], v[66:67]
	v_pk_mul_f32 v[68:69], v[72:73], v[68:69]
	v_pk_mul_f32 v[70:71], v[90:91], v[82:83] op_sel_hi:[0,1]
	v_pk_mul_f32 v[72:73], v[90:91], v[88:89] op_sel_hi:[0,1]
	v_pk_mul_f32 v[68:69], v[68:69], v[72:73]
	v_pk_mul_f32 v[66:67], v[66:67], v[70:71]
	v_med3_f32 v71, v74, s61, v237
	v_med3_f32 v72, v75, s61, v237
	v_mov_b32_e32 v70, v1
	v_cvt_pk_fp8_f32 v70, v71, v72
	v_med3_f32 v66, v66, s61, v237
	v_med3_f32 v67, v67, s61, v237
	v_mov_b32_e32 v71, v1
	v_cvt_pk_fp8_f32 v71, v66, v67
	v_pk_mul_f32 v[76:77], v[76:77], v[80:81]
	v_pk_mul_f32 v[80:81], v[90:91], v[84:85] op_sel_hi:[0,1]
	v_pk_mul_f32 v[76:77], v[76:77], v[80:81]
	v_med3_f32 v66, v68, s61, v237
	v_med3_f32 v73, v76, s61, v237
	v_med3_f32 v74, v77, s61, v237
	v_med3_f32 v67, v69, s61, v237
	v_cvt_pk_fp8_f32 v70, v73, v74 op_sel:[0,0,1]
	v_cvt_pk_fp8_f32 v71, v66, v67 op_sel:[0,0,1]
	v_cvt_f32_i32_e32 v59, v59
	v_cvt_f32_i32_e32 v58, v58
	v_mad_i64_i32 v[66:67], s[26:27], v91, s5, v[114:115]
	v_cvt_f32_i32_e32 v61, v61
	v_cvt_f32_i32_e32 v60, v60
	v_cvt_f32_i32_e32 v55, v55
	v_cvt_f32_i32_e32 v54, v54
	v_cvt_f32_i32_e32 v57, v57
	v_cvt_f32_i32_e32 v56, v56
	v_mul_f32_e32 v149, 0x3a800000, v149
	v_lshl_add_u64 v[66:67], v[66:67], 0, v[140:141]
	global_store_dwordx2 v[66:67], v[70:71], off
	v_mul_f32_e32 v66, 0xbfb8aa3b, v149
	v_pk_mul_f32 v[70:71], v[66:67], v[58:59] op_sel_hi:[0,1]
	v_pk_mul_f32 v[68:69], v[66:67], v[60:61] op_sel_hi:[0,1]
	v_pk_mul_f32 v[72:73], v[66:67], v[56:57] op_sel_hi:[0,1]
	v_pk_mul_f32 v[66:67], v[66:67], v[54:55] op_sel_hi:[0,1]
	v_exp_f32_e32 v70, v70
	v_exp_f32_e32 v71, v71
	v_exp_f32_e32 v66, v66
	v_exp_f32_e32 v67, v67
	v_exp_f32_e32 v72, v72
	v_exp_f32_e32 v73, v73
	v_pk_add_f32 v[70:71], v[70:71], 1.0 op_sel_hi:[1,0]
	v_cvt_f32_i32_e32 v63, v63
	v_cvt_f32_i32_e32 v62, v62
	v_exp_f32_e32 v68, v68
	v_exp_f32_e32 v69, v69
	v_pk_add_f32 v[72:73], v[72:73], 1.0 op_sel_hi:[1,0]
	v_pk_add_f32 v[66:67], v[66:67], 1.0 op_sel_hi:[1,0]
	v_rcp_f32_e32 v70, v70
	v_rcp_f32_e32 v71, v71
	v_cvt_f32_i32_e32 v53, v53
	v_cvt_f32_i32_e32 v52, v52
	v_cvt_f32_i32_e32 v51, v51
	v_cvt_f32_i32_e32 v50, v50
	v_rcp_f32_e32 v66, v66
	v_rcp_f32_e32 v67, v67
	v_rcp_f32_e32 v72, v72
	v_rcp_f32_e32 v73, v73
	v_mul_f32_e32 v74, v149, v149
	v_pk_add_f32 v[68:69], v[68:69], 1.0 op_sel_hi:[1,0]
	v_pk_mul_f32 v[58:59], v[58:59], v[62:63]
	v_pk_mul_f32 v[62:63], v[74:75], v[70:71] op_sel_hi:[0,1]
	v_cvt_f32_i32_e32 v65, v65
	v_cvt_f32_i32_e32 v64, v64
	v_rcp_f32_e32 v68, v68
	v_rcp_f32_e32 v69, v69
	v_pk_mul_f32 v[58:59], v[58:59], v[62:63]
	v_pk_mul_f32 v[50:51], v[54:55], v[50:51]
	v_pk_mul_f32 v[52:53], v[56:57], v[52:53]
	v_pk_mul_f32 v[54:55], v[74:75], v[66:67] op_sel_hi:[0,1]
	v_pk_mul_f32 v[56:57], v[74:75], v[72:73] op_sel_hi:[0,1]
	v_pk_mul_f32 v[52:53], v[52:53], v[56:57]
	v_pk_mul_f32 v[50:51], v[50:51], v[54:55]
	v_med3_f32 v55, v58, s61, v237
	v_med3_f32 v56, v59, s61, v237
	v_mov_b32_e32 v54, v1
	v_cvt_pk_fp8_f32 v54, v55, v56
	v_med3_f32 v50, v50, s61, v237
	v_med3_f32 v51, v51, s61, v237
	v_mov_b32_e32 v55, v1
	v_cvt_pk_fp8_f32 v55, v50, v51
	v_pk_mul_f32 v[60:61], v[60:61], v[64:65]
	v_pk_mul_f32 v[64:65], v[74:75], v[68:69] op_sel_hi:[0,1]
	v_pk_mul_f32 v[60:61], v[60:61], v[64:65]
	v_med3_f32 v50, v52, s61, v237
	v_med3_f32 v57, v60, s61, v237
	v_med3_f32 v58, v61, s61, v237
	v_med3_f32 v51, v53, s61, v237
	v_cvt_pk_fp8_f32 v54, v57, v58 op_sel:[0,0,1]
	v_cvt_pk_fp8_f32 v55, v50, v51 op_sel:[0,0,1]
	v_add_u32_e32 v148, 0x80, v142
	v_cvt_f32_i32_e32 v43, v43
	v_cvt_f32_i32_e32 v42, v42
	v_mad_i64_i32 v[50:51], s[26:27], v148, s5, v[114:115]
	v_cvt_f32_i32_e32 v45, v45
	v_cvt_f32_i32_e32 v44, v44
	v_cvt_f32_i32_e32 v39, v39
	v_cvt_f32_i32_e32 v38, v38
	v_cvt_f32_i32_e32 v41, v41
	v_cvt_f32_i32_e32 v40, v40
	v_lshl_add_u64 v[50:51], v[50:51], 0, v[140:141]
	global_store_dwordx2 v[50:51], v[54:55], off
	v_mul_f32_e32 v50, 0xbfb8aa3b, v147
	v_pk_mul_f32 v[54:55], v[50:51], v[42:43] op_sel_hi:[0,1]
	v_pk_mul_f32 v[52:53], v[50:51], v[44:45] op_sel_hi:[0,1]
	v_pk_mul_f32 v[56:57], v[50:51], v[40:41] op_sel_hi:[0,1]
	v_pk_mul_f32 v[50:51], v[50:51], v[38:39] op_sel_hi:[0,1]
	v_exp_f32_e32 v54, v54
	v_exp_f32_e32 v55, v55
	v_exp_f32_e32 v50, v50
	v_exp_f32_e32 v51, v51
	v_exp_f32_e32 v56, v56
	v_exp_f32_e32 v57, v57
	v_pk_add_f32 v[54:55], v[54:55], 1.0 op_sel_hi:[1,0]
	v_cvt_f32_i32_e32 v47, v47
	v_cvt_f32_i32_e32 v46, v46
	v_exp_f32_e32 v52, v52
	v_exp_f32_e32 v53, v53
	v_pk_add_f32 v[56:57], v[56:57], 1.0 op_sel_hi:[1,0]
	v_pk_add_f32 v[50:51], v[50:51], 1.0 op_sel_hi:[1,0]
	v_rcp_f32_e32 v54, v54
	v_rcp_f32_e32 v55, v55
	v_cvt_f32_i32_e32 v37, v37
	v_cvt_f32_i32_e32 v36, v36
	v_cvt_f32_i32_e32 v35, v35
	v_cvt_f32_i32_e32 v34, v34
	v_rcp_f32_e32 v50, v50
	v_rcp_f32_e32 v51, v51
	v_rcp_f32_e32 v56, v56
	v_rcp_f32_e32 v57, v57
	v_add_u32_e32 v59, 0x90, v142
	v_mul_f32_e32 v58, v147, v147
	v_pk_add_f32 v[52:53], v[52:53], 1.0 op_sel_hi:[1,0]
	v_pk_mul_f32 v[42:43], v[42:43], v[46:47]
	v_pk_mul_f32 v[46:47], v[58:59], v[54:55] op_sel_hi:[0,1]
	v_cvt_f32_i32_e32 v49, v49
	v_cvt_f32_i32_e32 v48, v48
	v_rcp_f32_e32 v52, v52
	v_rcp_f32_e32 v53, v53
	v_pk_mul_f32 v[42:43], v[42:43], v[46:47]
	v_pk_mul_f32 v[34:35], v[38:39], v[34:35]
	v_pk_mul_f32 v[36:37], v[40:41], v[36:37]
	v_pk_mul_f32 v[38:39], v[58:59], v[50:51] op_sel_hi:[0,1]
	v_pk_mul_f32 v[40:41], v[58:59], v[56:57] op_sel_hi:[0,1]
	v_pk_mul_f32 v[36:37], v[36:37], v[40:41]
	v_pk_mul_f32 v[34:35], v[34:35], v[38:39]
	v_med3_f32 v39, v42, s61, v237
	v_med3_f32 v40, v43, s61, v237
	v_mov_b32_e32 v38, v1
	v_cvt_pk_fp8_f32 v38, v39, v40
	v_med3_f32 v34, v34, s61, v237
	v_med3_f32 v35, v35, s61, v237
	v_mov_b32_e32 v39, v1
	v_cvt_pk_fp8_f32 v39, v34, v35
	v_pk_mul_f32 v[44:45], v[44:45], v[48:49]
	v_pk_mul_f32 v[48:49], v[58:59], v[52:53] op_sel_hi:[0,1]
	v_pk_mul_f32 v[44:45], v[44:45], v[48:49]
	v_med3_f32 v34, v36, s61, v237
	v_med3_f32 v41, v44, s61, v237
	v_med3_f32 v42, v45, s61, v237
	v_med3_f32 v35, v37, s61, v237
	v_cvt_pk_fp8_f32 v38, v41, v42 op_sel:[0,0,1]
	v_cvt_pk_fp8_f32 v39, v34, v35 op_sel:[0,0,1]
	v_cvt_f32_i32_e32 v27, v27
	v_cvt_f32_i32_e32 v26, v26
	v_mad_i64_i32 v[34:35], s[26:27], v59, s5, v[114:115]
	v_cvt_f32_i32_e32 v29, v29
	v_cvt_f32_i32_e32 v28, v28
	v_cvt_f32_i32_e32 v23, v23
	v_cvt_f32_i32_e32 v22, v22
	v_cvt_f32_i32_e32 v25, v25
	v_cvt_f32_i32_e32 v24, v24
	v_lshl_add_u64 v[34:35], v[34:35], 0, v[140:141]
	global_store_dwordx2 v[34:35], v[38:39], off
	v_mul_f32_e32 v34, 0xbfb8aa3b, v146
	v_pk_mul_f32 v[38:39], v[34:35], v[26:27] op_sel_hi:[0,1]
	v_pk_mul_f32 v[36:37], v[34:35], v[28:29] op_sel_hi:[0,1]
	v_pk_mul_f32 v[40:41], v[34:35], v[24:25] op_sel_hi:[0,1]
	v_pk_mul_f32 v[34:35], v[34:35], v[22:23] op_sel_hi:[0,1]
	v_exp_f32_e32 v38, v38
	v_exp_f32_e32 v39, v39
	v_exp_f32_e32 v34, v34
	v_exp_f32_e32 v35, v35
	v_exp_f32_e32 v40, v40
	v_exp_f32_e32 v41, v41
	v_pk_add_f32 v[38:39], v[38:39], 1.0 op_sel_hi:[1,0]
	v_cvt_f32_i32_e32 v31, v31
	v_cvt_f32_i32_e32 v30, v30
	v_exp_f32_e32 v36, v36
	v_exp_f32_e32 v37, v37
	v_pk_add_f32 v[40:41], v[40:41], 1.0 op_sel_hi:[1,0]
	v_pk_add_f32 v[34:35], v[34:35], 1.0 op_sel_hi:[1,0]
	v_rcp_f32_e32 v38, v38
	v_rcp_f32_e32 v39, v39
	v_cvt_f32_i32_e32 v21, v21
	v_cvt_f32_i32_e32 v20, v20
	v_cvt_f32_i32_e32 v19, v19
	v_cvt_f32_i32_e32 v18, v18
	v_rcp_f32_e32 v34, v34
	v_rcp_f32_e32 v35, v35
	v_rcp_f32_e32 v40, v40
	v_rcp_f32_e32 v41, v41
	v_add_u32_e32 v43, 0xa0, v142
	v_mul_f32_e32 v42, v146, v146
	v_pk_add_f32 v[36:37], v[36:37], 1.0 op_sel_hi:[1,0]
	v_pk_mul_f32 v[26:27], v[26:27], v[30:31]
	v_pk_mul_f32 v[30:31], v[42:43], v[38:39] op_sel_hi:[0,1]
	v_cvt_f32_i32_e32 v33, v33
	v_cvt_f32_i32_e32 v32, v32
	v_rcp_f32_e32 v36, v36
	v_rcp_f32_e32 v37, v37
	v_pk_mul_f32 v[26:27], v[26:27], v[30:31]
	v_pk_mul_f32 v[18:19], v[22:23], v[18:19]
	v_pk_mul_f32 v[20:21], v[24:25], v[20:21]
	v_pk_mul_f32 v[22:23], v[42:43], v[34:35] op_sel_hi:[0,1]
	v_pk_mul_f32 v[24:25], v[42:43], v[40:41] op_sel_hi:[0,1]
	v_pk_mul_f32 v[20:21], v[20:21], v[24:25]
	v_pk_mul_f32 v[18:19], v[18:19], v[22:23]
	v_med3_f32 v23, v26, s61, v237
	v_med3_f32 v24, v27, s61, v237
	v_mov_b32_e32 v22, v1
	v_cvt_pk_fp8_f32 v22, v23, v24
	v_med3_f32 v18, v18, s61, v237
	v_med3_f32 v19, v19, s61, v237
	v_mov_b32_e32 v23, v1
	v_cvt_pk_fp8_f32 v23, v18, v19
	v_pk_mul_f32 v[28:29], v[28:29], v[32:33]
	v_pk_mul_f32 v[32:33], v[42:43], v[36:37] op_sel_hi:[0,1]
	v_pk_mul_f32 v[28:29], v[28:29], v[32:33]
	v_med3_f32 v18, v20, s61, v237
	v_med3_f32 v25, v28, s61, v237
	v_med3_f32 v26, v29, s61, v237
	v_med3_f32 v19, v21, s61, v237
	v_cvt_pk_fp8_f32 v22, v25, v26 op_sel:[0,0,1]
	v_cvt_pk_fp8_f32 v23, v18, v19 op_sel:[0,0,1]
	v_cvt_f32_i32_e32 v11, v11
	v_cvt_f32_i32_e32 v10, v10
	v_mad_i64_i32 v[18:19], s[26:27], v43, s5, v[114:115]
	v_cvt_f32_i32_e32 v13, v13
	v_cvt_f32_i32_e32 v12, v12
	v_cvt_f32_i32_e32 v7, v7
	v_cvt_f32_i32_e32 v6, v6
	v_cvt_f32_i32_e32 v9, v9
	v_cvt_f32_i32_e32 v8, v8
	v_lshl_add_u64 v[18:19], v[18:19], 0, v[140:141]
	global_store_dwordx2 v[18:19], v[22:23], off
	v_mul_f32_e32 v18, 0xbfb8aa3b, v143
	v_pk_mul_f32 v[22:23], v[18:19], v[10:11] op_sel_hi:[0,1]
	v_pk_mul_f32 v[20:21], v[18:19], v[12:13] op_sel_hi:[0,1]
	v_pk_mul_f32 v[24:25], v[18:19], v[8:9] op_sel_hi:[0,1]
	v_pk_mul_f32 v[18:19], v[18:19], v[6:7] op_sel_hi:[0,1]
	v_exp_f32_e32 v22, v22
	v_exp_f32_e32 v23, v23
	v_exp_f32_e32 v18, v18
	v_exp_f32_e32 v19, v19
	v_exp_f32_e32 v24, v24
	v_exp_f32_e32 v25, v25
	v_pk_add_f32 v[22:23], v[22:23], 1.0 op_sel_hi:[1,0]
	v_cvt_f32_i32_e32 v15, v15
	v_cvt_f32_i32_e32 v14, v14
	v_exp_f32_e32 v20, v20
	v_exp_f32_e32 v21, v21
	v_pk_add_f32 v[24:25], v[24:25], 1.0 op_sel_hi:[1,0]
	v_pk_add_f32 v[18:19], v[18:19], 1.0 op_sel_hi:[1,0]
	v_rcp_f32_e32 v22, v22
	v_rcp_f32_e32 v23, v23
	v_cvt_f32_i32_e32 v5, v5
	v_cvt_f32_i32_e32 v4, v4
	v_cvt_f32_i32_e32 v3, v3
	v_cvt_f32_i32_e32 v2, v2
	v_rcp_f32_e32 v18, v18
	v_rcp_f32_e32 v19, v19
	v_rcp_f32_e32 v24, v24
	v_rcp_f32_e32 v25, v25
	v_add_u32_e32 v27, 0xb0, v142
	v_mul_f32_e32 v26, v143, v143
	v_pk_add_f32 v[20:21], v[20:21], 1.0 op_sel_hi:[1,0]
	v_pk_mul_f32 v[10:11], v[10:11], v[14:15]
	v_pk_mul_f32 v[14:15], v[26:27], v[22:23] op_sel_hi:[0,1]
	v_cvt_f32_i32_e32 v17, v17
	v_cvt_f32_i32_e32 v16, v16
	v_rcp_f32_e32 v20, v20
	v_rcp_f32_e32 v21, v21
	v_pk_mul_f32 v[10:11], v[10:11], v[14:15]
	v_pk_mul_f32 v[2:3], v[6:7], v[2:3]
	v_pk_mul_f32 v[4:5], v[8:9], v[4:5]
	v_pk_mul_f32 v[6:7], v[26:27], v[18:19] op_sel_hi:[0,1]
	v_pk_mul_f32 v[8:9], v[26:27], v[24:25] op_sel_hi:[0,1]
	v_pk_mul_f32 v[4:5], v[4:5], v[8:9]
	v_pk_mul_f32 v[2:3], v[2:3], v[6:7]
	v_med3_f32 v7, v10, s61, v237
	v_med3_f32 v8, v11, s61, v237
	v_mov_b32_e32 v6, v1
	v_cvt_pk_fp8_f32 v6, v7, v8
	v_med3_f32 v2, v2, s61, v237
	v_med3_f32 v3, v3, s61, v237
	v_mov_b32_e32 v7, v1
	v_cvt_pk_fp8_f32 v7, v2, v3
	v_pk_mul_f32 v[12:13], v[12:13], v[16:17]
	v_pk_mul_f32 v[16:17], v[26:27], v[20:21] op_sel_hi:[0,1]
	v_pk_mul_f32 v[12:13], v[12:13], v[16:17]
	v_med3_f32 v2, v4, s61, v237
	v_med3_f32 v9, v12, s61, v237
	v_med3_f32 v10, v13, s61, v237
	v_med3_f32 v3, v5, s61, v237
	v_cvt_pk_fp8_f32 v6, v9, v10 op_sel:[0,0,1]
	v_cvt_pk_fp8_f32 v7, v2, v3 op_sel:[0,0,1]
	v_mad_i64_i32 v[2:3], s[26:27], v27, s5, v[114:115]
	v_lshl_add_u64 v[2:3], v[2:3], 0, v[140:141]
	s_andn2_b64 vcc, exec, s[18:19]
	s_mov_b64 s[18:19], -1
	s_mov_b32 s76, s55
	s_mov_b32 s77, s65
	global_store_dwordx2 v[2:3], v[6:7], off
	s_cbranch_vccnz .LBB0_1166
	s_andn2_b64 vcc, exec, s[8:9]
	s_cbranch_vccnz .LBB0_1165
	s_barrier
	s_branch .LBB0_1165

.LBB0_1373:
	s_lshl_b32 s100, s59, 8
	s_add_i32 s100, s100, s40
	v_and_or_b32 v248, v234, 15, s100
	v_ashrrev_i32_e32 v249, 31, v248
	v_lshl_add_u64 v[248:249], v[248:249], 2, s[14:15]
	global_load_dword v240, v[248:249], off
	global_load_dword v241, v[248:249], off offset:64
	global_load_dword v242, v[248:249], off offset:128
	global_load_dword v243, v[248:249], off offset:192
	global_load_dword v244, v[248:249], off offset:512
	global_load_dword v245, v[248:249], off offset:576
	global_load_dword v246, v[248:249], off offset:640
	global_load_dword v247, v[248:249], off offset:704
	ds_read_b128 v[146:149], v140
	ds_read_b128 v[150:153], v140 offset:1024
	ds_read_b128 v[154:157], v140 offset:2048
	ds_read_b128 v[158:161], v140 offset:3072
	ds_read_b128 v[162:165], v141
	ds_read_b128 v[166:169], v141 offset:1024
	ds_read_b128 v[170:173], v141 offset:2048
	ds_read_b128 v[174:177], v141 offset:3072
	s_add_u32 s10, s26, 0xfffe0080
	s_addc_u32 s11, s27, -1
	s_cmp_eq_u32 s5, 4
	s_cselect_b32 s29, s21, s11
	s_cselect_b32 s28, s62, s10
	s_cselect_b32 s11, s19, s74
	s_cselect_b32 s10, s63, s80
	s_mov_b32 m0, s70
	v_lshl_add_u64 v[210:211], s[26:27], 0, v[136:137]
	ds_read_b128 v[178:181], v145
	ds_read_b128 v[182:185], v145 offset:1024
	ds_read_b128 v[186:189], v145 offset:2048
	ds_read_b128 v[190:193], v145 offset:3072
	ds_read_b128 v[194:197], v145 offset:4096
	ds_read_b128 v[198:201], v145 offset:5120
	ds_read_b128 v[202:205], v145 offset:6144
	ds_read_b128 v[206:209], v145 offset:7168
	global_load_lds_dwordx4 v[210:211], off
	v_lshl_add_u64 v[210:211], s[26:27], 0, v[138:139]
	s_mov_b32 m0, s4
	s_nop 0
	global_load_lds_dwordx4 v[210:211], off
	s_waitcnt vmcnt(16)
	s_waitcnt lgkmcnt(0)
	s_barrier
	s_setprio 1
	s_waitcnt lgkmcnt(0)
	v_mfma_i32_16x16x64_i8 v[122:125], v[146:149], v[178:181], v[122:125]
	v_mfma_i32_16x16x64_i8 v[118:121], v[154:157], v[178:181], v[118:121]
	v_mfma_i32_16x16x64_i8 v[106:109], v[146:149], v[186:189], v[106:109]
	v_mfma_i32_16x16x64_i8 v[102:105], v[154:157], v[186:189], v[102:105]
	v_mfma_i32_16x16x64_i8 v[90:93], v[146:149], v[194:197], v[90:93]
	v_mfma_i32_16x16x64_i8 v[86:89], v[154:157], v[194:197], v[86:89]
	v_mfma_i32_16x16x64_i8 v[74:77], v[146:149], v[202:205], v[74:77]
	v_mfma_i32_16x16x64_i8 v[70:73], v[154:157], v[202:205], v[70:73]
	v_mfma_i32_16x16x64_i8 v[122:125], v[150:153], v[182:185], v[122:125]
	v_mfma_i32_16x16x64_i8 v[118:121], v[158:161], v[182:185], v[118:121]
	v_mfma_i32_16x16x64_i8 v[106:109], v[150:153], v[190:193], v[106:109]
	v_mfma_i32_16x16x64_i8 v[102:105], v[158:161], v[190:193], v[102:105]
	v_mfma_i32_16x16x64_i8 v[90:93], v[150:153], v[198:201], v[90:93]
	v_mfma_i32_16x16x64_i8 v[86:89], v[158:161], v[198:201], v[86:89]
	v_mfma_i32_16x16x64_i8 v[74:77], v[150:153], v[206:209], v[74:77]
	v_mfma_i32_16x16x64_i8 v[70:73], v[158:161], v[206:209], v[70:73]
	s_setprio 0
	s_setprio 1
	v_mfma_i32_16x16x64_i8 v[126:129], v[162:165], v[178:181], v[126:129]
	v_mfma_i32_16x16x64_i8 v[114:117], v[170:173], v[178:181], v[114:117]
	v_mfma_i32_16x16x64_i8 v[110:113], v[162:165], v[186:189], v[110:113]
	v_mfma_i32_16x16x64_i8 v[98:101], v[170:173], v[186:189], v[98:101]
	v_mfma_i32_16x16x64_i8 v[94:97], v[162:165], v[194:197], v[94:97]
	v_mfma_i32_16x16x64_i8 v[82:85], v[170:173], v[194:197], v[82:85]
	v_mfma_i32_16x16x64_i8 v[78:81], v[162:165], v[202:205], v[78:81]
	v_mfma_i32_16x16x64_i8 v[66:69], v[170:173], v[202:205], v[66:69]
	v_mfma_i32_16x16x64_i8 v[126:129], v[166:169], v[182:185], v[126:129]
	v_mfma_i32_16x16x64_i8 v[114:117], v[174:177], v[182:185], v[114:117]
	v_mfma_i32_16x16x64_i8 v[110:113], v[166:169], v[190:193], v[110:113]
	v_mfma_i32_16x16x64_i8 v[98:101], v[174:177], v[190:193], v[98:101]
	v_mfma_i32_16x16x64_i8 v[94:97], v[166:169], v[198:201], v[94:97]
	v_mfma_i32_16x16x64_i8 v[82:85], v[174:177], v[198:201], v[82:85]
	v_mfma_i32_16x16x64_i8 v[78:81], v[166:169], v[206:209], v[78:81]
	v_mfma_i32_16x16x64_i8 v[66:69], v[174:177], v[206:209], v[66:69]
	s_setprio 0
	s_barrier
	s_mov_b32 m0, s50
	v_lshl_add_u64 v[210:211], s[10:11], 0, v[0:1]
	s_add_u32 s54, s10, 0x20000
	ds_read_b128 v[178:181], v145 offset:16384
	ds_read_b128 v[182:185], v145 offset:17408
	ds_read_b128 v[186:189], v145 offset:18432
	ds_read_b128 v[190:193], v145 offset:19456
	ds_read_b128 v[194:197], v145 offset:20480
	ds_read_b128 v[198:201], v145 offset:21504
	ds_read_b128 v[202:205], v145 offset:22528
	ds_read_b128 v[206:209], v145 offset:23552
	global_load_lds_dwordx4 v[210:211], off
	v_lshl_add_u64 v[212:213], s[10:11], 0, v[130:131]
	s_mov_b32 m0, s51
	s_addc_u32 s55, s11, 0
	global_load_lds_dwordx4 v[212:213], off
	v_lshl_add_u64 v[214:215], s[54:55], 0, v[0:1]
	s_mov_b32 m0, s71
	v_lshl_add_u64 v[216:217], s[28:29], 0, v[132:133]
	global_load_lds_dwordx4 v[214:215], off
	v_lshl_add_u64 v[214:215], s[54:55], 0, v[130:131]
	s_mov_b32 m0, s75
	s_nop 0
	global_load_lds_dwordx4 v[214:215], off
	v_lshl_add_u64 v[214:215], s[28:29], 0, v[134:135]
	s_mov_b32 m0, s36
	s_nop 0
	global_load_lds_dwordx4 v[214:215], off
	s_mov_b32 m0, s37
	s_nop 0
	global_load_lds_dwordx4 v[216:217], off
	s_waitcnt vmcnt(16)
	s_waitcnt lgkmcnt(0)
	s_barrier
	s_setprio 1
	s_waitcnt lgkmcnt(0)
	v_mfma_i32_16x16x64_i8 v[58:61], v[146:149], v[178:181], v[58:61]
	v_mfma_i32_16x16x64_i8 v[54:57], v[154:157], v[178:181], v[54:57]
	v_mfma_i32_16x16x64_i8 v[42:45], v[146:149], v[186:189], v[42:45]
	v_mfma_i32_16x16x64_i8 v[38:41], v[154:157], v[186:189], v[38:41]
	v_mfma_i32_16x16x64_i8 v[26:29], v[146:149], v[194:197], v[26:29]
	v_mfma_i32_16x16x64_i8 v[22:25], v[154:157], v[194:197], v[22:25]
	v_mfma_i32_16x16x64_i8 v[10:13], v[146:149], v[202:205], v[10:13]
	v_mfma_i32_16x16x64_i8 v[6:9], v[154:157], v[202:205], v[6:9]
	v_mfma_i32_16x16x64_i8 v[58:61], v[150:153], v[182:185], v[58:61]
	v_mfma_i32_16x16x64_i8 v[54:57], v[158:161], v[182:185], v[54:57]
	v_mfma_i32_16x16x64_i8 v[42:45], v[150:153], v[190:193], v[42:45]
	v_mfma_i32_16x16x64_i8 v[38:41], v[158:161], v[190:193], v[38:41]
	v_mfma_i32_16x16x64_i8 v[26:29], v[150:153], v[198:201], v[26:29]
	v_mfma_i32_16x16x64_i8 v[22:25], v[158:161], v[198:201], v[22:25]
	v_mfma_i32_16x16x64_i8 v[10:13], v[150:153], v[206:209], v[10:13]
	v_mfma_i32_16x16x64_i8 v[6:9], v[158:161], v[206:209], v[6:9]
	s_setprio 0
	s_setprio 1
	v_mfma_i32_16x16x64_i8 v[62:65], v[162:165], v[178:181], v[62:65]
	v_mfma_i32_16x16x64_i8 v[50:53], v[170:173], v[178:181], v[50:53]
	v_mfma_i32_16x16x64_i8 v[46:49], v[162:165], v[186:189], v[46:49]
	v_mfma_i32_16x16x64_i8 v[34:37], v[170:173], v[186:189], v[34:37]
	v_mfma_i32_16x16x64_i8 v[30:33], v[162:165], v[194:197], v[30:33]
	v_mfma_i32_16x16x64_i8 v[18:21], v[170:173], v[194:197], v[18:21]
	v_mfma_i32_16x16x64_i8 v[14:17], v[162:165], v[202:205], v[14:17]
	v_mfma_i32_16x16x64_i8 v[2:5], v[170:173], v[202:205], v[2:5]
	v_mfma_i32_16x16x64_i8 v[62:65], v[166:169], v[182:185], v[62:65]
	v_mfma_i32_16x16x64_i8 v[50:53], v[174:177], v[182:185], v[50:53]
	v_mfma_i32_16x16x64_i8 v[46:49], v[166:169], v[190:193], v[46:49]
	v_mfma_i32_16x16x64_i8 v[34:37], v[174:177], v[190:193], v[34:37]
	v_mfma_i32_16x16x64_i8 v[30:33], v[166:169], v[198:201], v[30:33]
	v_mfma_i32_16x16x64_i8 v[18:21], v[174:177], v[198:201], v[18:21]
	v_mfma_i32_16x16x64_i8 v[14:17], v[166:169], v[206:209], v[14:17]
	v_mfma_i32_16x16x64_i8 v[2:5], v[174:177], v[206:209], v[2:5]
	s_setprio 0
	s_barrier
	ds_read_b128 v[146:149], v142
	ds_read_b128 v[150:153], v142 offset:1024
	ds_read_b128 v[154:157], v142 offset:2048
	ds_read_b128 v[158:161], v142 offset:3072
	ds_read_b128 v[162:165], v143
	ds_read_b128 v[166:169], v143 offset:1024
	ds_read_b128 v[170:173], v143 offset:2048
	ds_read_b128 v[174:177], v143 offset:3072
	s_add_u32 s28, s28, 0x20000
	s_addc_u32 s29, s29, 0
	s_mov_b32 m0, s38
	v_lshl_add_u64 v[218:219], s[28:29], 0, v[134:135]
	ds_read_b128 v[178:181], v145 offset:32768
	ds_read_b128 v[182:185], v145 offset:33792
	ds_read_b128 v[186:189], v145 offset:34816
	ds_read_b128 v[190:193], v145 offset:35840
	ds_read_b128 v[194:197], v145 offset:36864
	ds_read_b128 v[198:201], v145 offset:37888
	ds_read_b128 v[202:205], v145 offset:38912
	ds_read_b128 v[206:209], v145 offset:39936
	global_load_lds_dwordx4 v[218:219], off
	v_lshl_add_u64 v[218:219], s[28:29], 0, v[132:133]
	s_mov_b32 m0, s39
	s_nop 0
	global_load_lds_dwordx4 v[218:219], off
	s_waitcnt vmcnt(8)
	s_waitcnt lgkmcnt(0)
	s_barrier
	s_setprio 1
	s_waitcnt lgkmcnt(0)
	v_mfma_i32_16x16x64_i8 v[122:125], v[146:149], v[178:181], v[122:125]
	v_mfma_i32_16x16x64_i8 v[118:121], v[154:157], v[178:181], v[118:121]
	v_mfma_i32_16x16x64_i8 v[106:109], v[146:149], v[186:189], v[106:109]
	v_mfma_i32_16x16x64_i8 v[102:105], v[154:157], v[186:189], v[102:105]
	v_mfma_i32_16x16x64_i8 v[90:93], v[146:149], v[194:197], v[90:93]
	v_mfma_i32_16x16x64_i8 v[86:89], v[154:157], v[194:197], v[86:89]
	v_mfma_i32_16x16x64_i8 v[74:77], v[146:149], v[202:205], v[74:77]
	v_mfma_i32_16x16x64_i8 v[70:73], v[154:157], v[202:205], v[70:73]
	v_mfma_i32_16x16x64_i8 v[122:125], v[150:153], v[182:185], v[122:125]
	v_mfma_i32_16x16x64_i8 v[118:121], v[158:161], v[182:185], v[118:121]
	v_mfma_i32_16x16x64_i8 v[106:109], v[150:153], v[190:193], v[106:109]
	v_mfma_i32_16x16x64_i8 v[102:105], v[158:161], v[190:193], v[102:105]
	v_mfma_i32_16x16x64_i8 v[90:93], v[150:153], v[198:201], v[90:93]
	v_mfma_i32_16x16x64_i8 v[86:89], v[158:161], v[198:201], v[86:89]
	v_mfma_i32_16x16x64_i8 v[74:77], v[150:153], v[206:209], v[74:77]
	v_mfma_i32_16x16x64_i8 v[70:73], v[158:161], v[206:209], v[70:73]
	s_setprio 0
	s_setprio 1
	v_mfma_i32_16x16x64_i8 v[126:129], v[162:165], v[178:181], v[126:129]
	v_mfma_i32_16x16x64_i8 v[114:117], v[170:173], v[178:181], v[114:117]
	v_mfma_i32_16x16x64_i8 v[110:113], v[162:165], v[186:189], v[110:113]
	v_mfma_i32_16x16x64_i8 v[98:101], v[170:173], v[186:189], v[98:101]
	v_mfma_i32_16x16x64_i8 v[94:97], v[162:165], v[194:197], v[94:97]
	v_mfma_i32_16x16x64_i8 v[82:85], v[170:173], v[194:197], v[82:85]
	v_mfma_i32_16x16x64_i8 v[78:81], v[162:165], v[202:205], v[78:81]
	v_mfma_i32_16x16x64_i8 v[66:69], v[170:173], v[202:205], v[66:69]
	v_mfma_i32_16x16x64_i8 v[126:129], v[166:169], v[182:185], v[126:129]
	v_mfma_i32_16x16x64_i8 v[114:117], v[174:177], v[182:185], v[114:117]
	v_mfma_i32_16x16x64_i8 v[110:113], v[166:169], v[190:193], v[110:113]
	v_mfma_i32_16x16x64_i8 v[98:101], v[174:177], v[190:193], v[98:101]
	v_mfma_i32_16x16x64_i8 v[94:97], v[166:169], v[198:201], v[94:97]
	v_mfma_i32_16x16x64_i8 v[82:85], v[174:177], v[198:201], v[82:85]
	v_mfma_i32_16x16x64_i8 v[78:81], v[166:169], v[206:209], v[78:81]
	v_mfma_i32_16x16x64_i8 v[66:69], v[174:177], v[206:209], v[66:69]
	s_setprio 0
	s_barrier
	s_mov_b32 m0, s78
	v_lshl_add_u64 v[210:211], v[210:211], 0, s[56:57]
	s_add_u32 s10, s10, 0x20080
	ds_read_b128 v[178:181], v145 offset:49152
	ds_read_b128 v[182:185], v145 offset:50176
	ds_read_b128 v[186:189], v145 offset:51200
	ds_read_b128 v[190:193], v145 offset:52224
	ds_read_b128 v[194:197], v145 offset:53248
	ds_read_b128 v[198:201], v145 offset:54272
	ds_read_b128 v[202:205], v145 offset:55296
	ds_read_b128 v[206:209], v145 offset:56320
	global_load_lds_dwordx4 v[210:211], off
	v_lshl_add_u64 v[210:211], v[212:213], 0, s[56:57]
	s_mov_b32 m0, s79
	s_addc_u32 s11, s11, 0
	global_load_lds_dwordx4 v[210:211], off
	v_lshl_add_u64 v[210:211], s[10:11], 0, v[0:1]
	s_mov_b32 m0, s58
	s_nop 0
	global_load_lds_dwordx4 v[210:211], off
	v_lshl_add_u64 v[210:211], s[10:11], 0, v[130:131]
	s_mov_b32 m0, s48
	s_nop 0
	global_load_lds_dwordx4 v[210:211], off
	v_lshl_add_u64 v[210:211], v[214:215], 0, s[56:57]
	s_mov_b32 m0, s45
	s_nop 0
	global_load_lds_dwordx4 v[210:211], off
	v_lshl_add_u64 v[210:211], v[216:217], 0, s[56:57]
	s_mov_b32 m0, s49
	s_nop 0
	global_load_lds_dwordx4 v[210:211], off
	s_waitcnt vmcnt(8)
	s_waitcnt lgkmcnt(0)
	s_barrier
	s_setprio 1
	s_waitcnt lgkmcnt(0)
	v_mfma_i32_16x16x64_i8 v[58:61], v[146:149], v[178:181], v[58:61]
	v_mfma_i32_16x16x64_i8 v[54:57], v[154:157], v[178:181], v[54:57]
	v_mfma_i32_16x16x64_i8 v[42:45], v[146:149], v[186:189], v[42:45]
	v_mfma_i32_16x16x64_i8 v[38:41], v[154:157], v[186:189], v[38:41]
	v_mfma_i32_16x16x64_i8 v[26:29], v[146:149], v[194:197], v[26:29]
	v_mfma_i32_16x16x64_i8 v[22:25], v[154:157], v[194:197], v[22:25]
	v_mfma_i32_16x16x64_i8 v[10:13], v[146:149], v[202:205], v[10:13]
	v_mfma_i32_16x16x64_i8 v[6:9], v[154:157], v[202:205], v[6:9]
	v_mfma_i32_16x16x64_i8 v[58:61], v[150:153], v[182:185], v[58:61]
	v_mfma_i32_16x16x64_i8 v[54:57], v[158:161], v[182:185], v[54:57]
	v_mfma_i32_16x16x64_i8 v[42:45], v[150:153], v[190:193], v[42:45]
	v_mfma_i32_16x16x64_i8 v[38:41], v[158:161], v[190:193], v[38:41]
	v_mfma_i32_16x16x64_i8 v[26:29], v[150:153], v[198:201], v[26:29]
	v_mfma_i32_16x16x64_i8 v[22:25], v[158:161], v[198:201], v[22:25]
	v_mfma_i32_16x16x64_i8 v[10:13], v[150:153], v[206:209], v[10:13]
	v_mfma_i32_16x16x64_i8 v[6:9], v[158:161], v[206:209], v[6:9]
	s_setprio 0
	s_setprio 1
	v_mfma_i32_16x16x64_i8 v[62:65], v[162:165], v[178:181], v[62:65]
	v_mfma_i32_16x16x64_i8 v[50:53], v[170:173], v[178:181], v[50:53]
	v_mfma_i32_16x16x64_i8 v[46:49], v[162:165], v[186:189], v[46:49]
	v_mfma_i32_16x16x64_i8 v[34:37], v[170:173], v[186:189], v[34:37]
	v_mfma_i32_16x16x64_i8 v[30:33], v[162:165], v[194:197], v[30:33]
	v_mfma_i32_16x16x64_i8 v[18:21], v[170:173], v[194:197], v[18:21]
	v_mfma_i32_16x16x64_i8 v[14:17], v[162:165], v[202:205], v[14:17]
	v_mfma_i32_16x16x64_i8 v[2:5], v[170:173], v[202:205], v[2:5]
	v_mfma_i32_16x16x64_i8 v[62:65], v[166:169], v[182:185], v[62:65]
	v_mfma_i32_16x16x64_i8 v[50:53], v[174:177], v[182:185], v[50:53]
	v_mfma_i32_16x16x64_i8 v[46:49], v[166:169], v[190:193], v[46:49]
	v_mfma_i32_16x16x64_i8 v[34:37], v[174:177], v[190:193], v[34:37]
	v_mfma_i32_16x16x64_i8 v[30:33], v[166:169], v[198:201], v[30:33]
	v_mfma_i32_16x16x64_i8 v[18:21], v[174:177], v[198:201], v[18:21]
	v_mfma_i32_16x16x64_i8 v[14:17], v[166:169], v[206:209], v[14:17]
	v_mfma_i32_16x16x64_i8 v[2:5], v[174:177], v[206:209], v[2:5]
	s_setprio 0
	s_barrier
	s_add_i32 s5, s5, 2
	s_add_u32 s26, s26, 0x100
	s_addc_u32 s27, s27, 0
	s_add_u32 s80, s80, 0x100
	s_addc_u32 s74, s74, 0
	s_cmp_gt_u32 s5, 5
	s_cbranch_scc0 .LBB0_1373
	s_lshl_b32 s4, s59, 8
	s_add_i32 s4, s4, s40
	v_mbcnt_lo_u32_b32 v140, -1, 0
	v_mbcnt_hi_u32_b32 v140, -1, v140
	s_and_b64 vcc, exec, s[16:17]
	v_and_or_b32 v142, v140, 15, s4
	v_ashrrev_i32_e32 v143, 31, v142
	v_lshl_add_u64 v[152:153], v[142:143], 2, s[14:15]
	v_mov_b32_e32 v141, v240
	v_mov_b32_e32 v151, v241
	v_mov_b32_e32 v150, v242
	v_mov_b32_e32 v149, v243
	v_mov_b32_e32 v148, v244
	v_mov_b32_e32 v147, v245
	v_mov_b32_e32 v146, v246
	v_mov_b32_e32 v143, v247
	s_cbranch_vccz .LBB0_1376
	s_barrier
.LBB0_1376:
	v_cvt_f32_i32_e32 v123, v123
	v_cvt_f32_i32_e32 v122, v122
	v_cvt_f32_i32_e32 v125, v125
	v_cvt_f32_i32_e32 v124, v124
	v_cvt_f32_i32_e32 v119, v119
	v_cvt_f32_i32_e32 v118, v118
	v_cvt_f32_i32_e32 v121, v121
	v_cvt_f32_i32_e32 v120, v120
	s_waitcnt vmcnt(8)
	v_mul_f32_e32 v164, 0x3a800000, v141
	v_mul_f32_e32 v152, 0xbfb8aa3b, v164
	v_pk_mul_f32 v[156:157], v[152:153], v[122:123] op_sel_hi:[0,1]
	v_pk_mul_f32 v[154:155], v[152:153], v[124:125] op_sel_hi:[0,1]
	v_pk_mul_f32 v[158:159], v[152:153], v[120:121] op_sel_hi:[0,1]
	v_pk_mul_f32 v[152:153], v[152:153], v[118:119] op_sel_hi:[0,1]
	v_exp_f32_e32 v156, v156
	v_exp_f32_e32 v157, v157
	v_exp_f32_e32 v152, v152
	v_exp_f32_e32 v153, v153
	v_exp_f32_e32 v154, v154
	v_exp_f32_e32 v155, v155
	s_mul_hi_i32 s4, s44, 0x2e8ba2e9
	v_exp_f32_e32 v158, v158
	v_exp_f32_e32 v159, v159
	s_lshr_b32 s5, s4, 31
	s_lshr_b32 s4, s4, 2
	s_add_i32 s4, s4, s5
	v_cvt_f32_i32_e32 v161, v117
	v_cvt_f32_i32_e32 v160, v116
	v_pk_add_f32 v[116:117], v[156:157], 1.0 op_sel_hi:[1,0]
	s_mul_i32 s4, s4, 22
	v_cvt_f32_i32_e32 v127, v127
	v_cvt_f32_i32_e32 v126, v126
	v_cvt_f32_i32_e32 v163, v115
	v_cvt_f32_i32_e32 v162, v114
	v_pk_add_f32 v[114:115], v[154:155], 1.0 op_sel_hi:[1,0]
	v_pk_add_f32 v[152:153], v[152:153], 1.0 op_sel_hi:[1,0]
	v_rcp_f32_e32 v116, v116
	v_rcp_f32_e32 v117, v117
	s_sub_i32 s4, s44, s4
	v_cvt_f32_i32_e32 v129, v129
	v_cvt_f32_i32_e32 v128, v128
	v_pk_add_f32 v[154:155], v[158:159], 1.0 op_sel_hi:[1,0]
	v_rcp_f32_e32 v152, v152
	v_rcp_f32_e32 v153, v153
	v_rcp_f32_e32 v114, v114
	v_rcp_f32_e32 v115, v115
	v_ashrrev_i32_e32 v140, 1, v140
	s_lshl_b32 s4, s4, 7
	v_rcp_f32_e32 v154, v154
	v_rcp_f32_e32 v155, v155
	v_and_b32_e32 v140, -8, v140
	s_or_b32 s4, s4, s41
	v_mul_f32_e32 v156, v164, v164
	v_add_u32_e32 v140, s4, v140
	v_pk_mul_f32 v[122:123], v[122:123], v[126:127]
	v_pk_mul_f32 v[116:117], v[156:157], v[116:117] op_sel_hi:[0,1]
	v_readlane_b32 s4, v255, 23
	v_pk_mul_f32 v[124:125], v[124:125], v[128:129]
	v_pk_mul_f32 v[114:115], v[156:157], v[114:115] op_sel_hi:[0,1]
	v_pk_mul_f32 v[116:117], v[122:123], v[116:117]
	v_pk_mul_f32 v[122:123], v[118:119], v[162:163]
	v_pk_mul_f32 v[118:119], v[120:121], v[160:161]
	v_pk_mul_f32 v[120:121], v[156:157], v[152:153] op_sel_hi:[0,1]
	v_readlane_b32 s5, v255, 24
	v_pk_mul_f32 v[114:115], v[124:125], v[114:115]
	v_pk_mul_f32 v[124:125], v[156:157], v[154:155] op_sel_hi:[0,1]
	v_pk_mul_f32 v[120:121], v[122:123], v[120:121]
	v_cndmask_b32_e64 v122, 0, 1, s[4:5]
	v_readlane_b32 s62, v255, 11
	v_readlane_b32 s78, v255, 13
	v_ashrrev_i32_e32 v141, 31, v140
	v_pk_mul_f32 v[118:119], v[118:119], v[124:125]
	v_cmp_ne_u32_e64 s[10:11], 1, v122
	s_andn2_b64 vcc, exec, s[4:5]
	s_mov_b64 s[26:27], -1
	v_readlane_b32 s63, v255, 12
	v_readlane_b32 s79, v255, 14
	s_movk_i32 s19, 0xb00
	s_movk_i32 s21, 0x1600
	s_movk_i32 s74, 0x1000
	s_cbranch_vccnz .LBB0_1378
	v_max_f32_e32 v122, v116, v116
	v_med3_f32 v123, v122, s61, v237
	v_max_f32_e32 v122, v117, v117
	v_med3_f32 v124, v122, s61, v237
	v_mov_b32_e32 v122, v1
	v_cvt_pk_fp8_f32 v122, v123, v124
	v_max_f32_e32 v125, v114, v114
	v_max_f32_e32 v124, v115, v115
	v_med3_f32 v123, v125, s61, v237
	v_med3_f32 v124, v124, s61, v237
	v_cvt_pk_fp8_f32 v122, v123, v124 op_sel:[0,0,1]
	v_max_f32_e32 v123, v120, v120
	v_med3_f32 v124, v123, s61, v237
	v_max_f32_e32 v123, v121, v121
	v_med3_f32 v125, v123, s61, v237
	v_mov_b32_e32 v123, v1
	v_cvt_pk_fp8_f32 v123, v124, v125
	v_max_f32_e32 v126, v118, v118
	v_max_f32_e32 v125, v119, v119
	v_med3_f32 v124, v126, s61, v237
	v_med3_f32 v125, v125, s61, v237
	v_cvt_pk_fp8_f32 v123, v124, v125 op_sel:[0,0,1]
	v_mov_b64_e32 v[124:125], s[12:13]
	v_mad_i64_i32 v[124:125], s[4:5], v142, s19, v[124:125]
	v_lshl_add_u64 v[124:125], v[124:125], 0, v[140:141]
	s_mov_b64 s[26:27], 0
	global_store_dwordx2 v[124:125], v[122:123], off
